# FFN-in phase start: workgroups with bit 3 of their id set sleep ~3400 clocks so that the workgroups sharing a streamed tile run one k-step apart
# speedup vs baseline: 1.0241x; 1.0086x over previous
.LBB0_215:
	v_readlane_b32 s98, v254, 31
	s_bitcmp1_b32 s98, 3
	s_cbranch_scc0 .Lstg_0
	s_sleep 53
